# speedup vs baseline: 1.0079x; 1.0079x over previous
_Z16sum_layer_kernelPKfS0_Pf:
	s_load_dwordx4 s[4:7], s[0:1], 0x0
	s_load_dwordx2 s[8:9], s[0:1], 0x10
	s_and_b32 s40, s2, 7
	s_lshl_b32 s40, s40, 2
	s_lshr_b32 s41, s2, 3
	s_and_b32 s42, s41, 3
	s_or_b32 s40, s40, s42
	s_lshr_b32 s41, s41, 2
	s_lshl_b32 s41, s41, 5
	s_or_b32 s2, s40, s41
	v_and_b32_e32 v40, 31, v0
	v_bfe_u32 v41, v0, 5, 1
	v_lshrrev_b32_e32 v42, 6, v0
	v_and_b32_e32 v43, 7, v0
	v_bfe_u32 v44, v0, 3, 3
	v_and_b32_e32 v45, 63, v0
	s_lshl_b32 s3, s2, 12
	s_lshl_b32 s19, s2, 7
	v_lshlrev_b32_e32 v1, 11, v41
	v_lshl_or_b32 v1, v40, 2, v1
	v_lshlrev_b32_e32 v46, 4, v43
	v_lshl_add_u32 v35, v44, 16, v46
	v_lshl_add_u32 v35, v42, 21, v35
	v_add_u32_e32 v35, s19, v35
	v_lshlrev_b32_e32 v36, 2, v40
	v_lshl_add_u32 v36, v41, 18, v36
	v_lshl_add_u32 v36, v42, 21, v36
	v_add_u32_e32 v36, s19, v36
	v_mul_u32_u24_e32 v37, 0x1200, v42
	v_mul_u32_u24_e32 v38, 0x90, v44
	v_add3_u32 v38, v37, v38, v46
	v_mul_u32_u24_e32 v39, 0x90, v40
	v_lshlrev_b32_e32 v47, 6, v41
	v_add3_u32 v39, v37, v39, v47
	v_lshrrev_b32_e32 v46, 1, v44
	v_xor_b32_e32 v46, v43, v46
	v_lshlrev_b32_e32 v46, 4, v46
	v_lshl_add_u32 v35, v44, 16, v46
	v_lshl_add_u32 v35, v42, 21, v35
	v_add_u32_e32 v35, s19, v35
	v_xor_b32_e32 v86, 64, v35
	v_readfirstlane_b32 s23, v42
	v_bfe_u32 v47, v40, 1, 3
	v_lshlrev_b32_e32 v39, 2, v41
	v_xor_b32_e32 v39, v39, v47
	s_lshl_b32 s23, s23, 12
	v_lshlrev_b32_e32 v39, 4, v39
	v_lshl_add_u32 v39, v40, 7, v39
	v_lshl_add_u32 v39, v42, 12, v39
	s_mov_b32 m0, s23
	v_xor_b32_e32 v81, 16, v39
	v_xor_b32_e32 v82, 32, v39
	v_xor_b32_e32 v83, 48, v39
	v_cmp_gt_u32_e32 vcc, 32, v45
	v_mov_b32_e32 v34, 0xc1600000
	v_mov_b32_e32 v84, 0x3fb8aa3b
	v_mov_b32_e32 v85, 0x3f317218
	s_mov_b32 s16, 0x3fb8aa3b
	s_mov_b32 s17, 0x3f317218
	s_mov_b32 s20, 0x7fc00
	s_mov_b32 s21, 0xff800
	s_mov_b32 s22, 0x17f400
	s_lshl_b32 s24, 1, 16
	s_lshl_b32 s25, 2, 16
	s_lshl_b32 s26, 3, 16
	s_lshl_b32 s27, 8, 16
	s_lshl_b32 s28, 9, 16
	s_lshl_b32 s29, 10, 16
	s_lshl_b32 s30, 11, 16
	s_lshl_b32 s31, 16, 16
	s_lshl_b32 s32, 17, 16
	s_lshl_b32 s33, 18, 16
	s_lshl_b32 s34, 19, 16
	s_lshl_b32 s35, 24, 16
	s_lshl_b32 s36, 25, 16
	s_lshl_b32 s37, 26, 16
	s_lshl_b32 s38, 27, 16
	s_mov_b32 s14, 0x200000
	s_mov_b32 s15, 0x20000
	s_waitcnt lgkmcnt(0)
	s_mov_b32 s12, s6
	s_and_b32 s13, s7, 0xffff
	s_and_b32 s5, s5, 0xffff
	s_mov_b32 s6, 0x800000
	s_mov_b32 s7, s15
	s_and_b32 s9, s9, 0xffff
	s_mov_b32 s10, s6
	s_mov_b32 s11, s15
	buffer_load_dword v18, v1, s[12:15], s3 offen nt
	buffer_load_dword v19, v1, s[12:15], s3 offen offset:128 nt
	buffer_load_dword v20, v1, s[12:15], s3 offen offset:256 nt
	buffer_load_dword v21, v1, s[12:15], s3 offen offset:384 nt
	buffer_load_dword v22, v1, s[12:15], s3 offen offset:512 nt
	buffer_load_dword v23, v1, s[12:15], s3 offen offset:640 nt
	buffer_load_dword v24, v1, s[12:15], s3 offen offset:768 nt
	buffer_load_dword v25, v1, s[12:15], s3 offen offset:896 nt
	buffer_load_dword v26, v1, s[12:15], s3 offen offset:1024 nt
	buffer_load_dword v27, v1, s[12:15], s3 offen offset:1152 nt
	buffer_load_dword v28, v1, s[12:15], s3 offen offset:1280 nt
	buffer_load_dword v29, v1, s[12:15], s3 offen offset:1408 nt
	buffer_load_dword v30, v1, s[12:15], s3 offen offset:1536 nt
	buffer_load_dword v31, v1, s[12:15], s3 offen offset:1664 nt
	buffer_load_dword v32, v1, s[12:15], s3 offen offset:1792 nt
	buffer_load_dword v33, v1, s[12:15], s3 offen offset:1920 nt
	buffer_load_dwordx4 v35, s[4:7], 0 offen nt lds
	buffer_load_dwordx4 v86, s[4:7], s20 offen offset:1024 nt lds
	buffer_load_dwordx4 v35, s[4:7], s21 offen offset:2048 nt lds
	buffer_load_dwordx4 v86, s[4:7], s22 offen offset:3072 nt lds
	s_waitcnt vmcnt(4)
	v_max3_f32 v48, v18, v19, v20
	v_max3_f32 v50, v21, v22, v23
	v_max3_f32 v48, v48, v24, v25
	v_max3_f32 v50, v50, v26, v27
	v_max3_f32 v48, v48, v28, v29
	v_max3_f32 v50, v50, v30, v31
	v_max3_f32 v48, v48, v32, v33
	v_max_f32_e32 v48, v48, v50
	v_mov_b32_e32 v50, v48
	s_nop 1
	v_permlane32_swap_b32_e32 v48, v50
	v_max_f32_e32 v48, v48, v50
	v_fmamk_f32 v48, v48, 0x3fb8aa3b, v34
	v_pk_fma_f32 v[18:19], v[18:19], v[84:85], v[48:49] op_sel_hi:[1,0,0] neg_lo:[0,0,1] neg_hi:[0,0,1]
	v_exp_f32_e32 v18, v18
	v_exp_f32_e32 v19, v19
	v_pk_fma_f32 v[20:21], v[20:21], v[84:85], v[48:49] op_sel_hi:[1,0,0] neg_lo:[0,0,1] neg_hi:[0,0,1]
	v_exp_f32_e32 v20, v20
	v_exp_f32_e32 v21, v21
	v_pk_fma_f32 v[22:23], v[22:23], v[84:85], v[48:49] op_sel_hi:[1,0,0] neg_lo:[0,0,1] neg_hi:[0,0,1]
	v_exp_f32_e32 v22, v22
	v_exp_f32_e32 v23, v23
	v_pk_fma_f32 v[24:25], v[24:25], v[84:85], v[48:49] op_sel_hi:[1,0,0] neg_lo:[0,0,1] neg_hi:[0,0,1]
	v_exp_f32_e32 v24, v24
	v_exp_f32_e32 v25, v25
	v_pk_fma_f32 v[26:27], v[26:27], v[84:85], v[48:49] op_sel_hi:[1,0,0] neg_lo:[0,0,1] neg_hi:[0,0,1]
	v_exp_f32_e32 v26, v26
	v_exp_f32_e32 v27, v27
	v_pk_fma_f32 v[28:29], v[28:29], v[84:85], v[48:49] op_sel_hi:[1,0,0] neg_lo:[0,0,1] neg_hi:[0,0,1]
	v_exp_f32_e32 v28, v28
	v_exp_f32_e32 v29, v29
	v_pk_fma_f32 v[30:31], v[30:31], v[84:85], v[48:49] op_sel_hi:[1,0,0] neg_lo:[0,0,1] neg_hi:[0,0,1]
	v_exp_f32_e32 v30, v30
	v_exp_f32_e32 v31, v31
	v_pk_fma_f32 v[32:33], v[32:33], v[84:85], v[48:49] op_sel_hi:[1,0,0] neg_lo:[0,0,1] neg_hi:[0,0,1]
	v_exp_f32_e32 v32, v32
	v_exp_f32_e32 v33, v33
	v_pk_add_f32 v[56:57], v[18:19], v[20:21]
	v_pk_add_f32 v[58:59], v[22:23], v[24:25]
	v_pk_add_f32 v[60:61], v[26:27], v[28:29]
	v_pk_add_f32 v[62:63], v[30:31], v[32:33]
	v_pk_add_f32 v[56:57], v[56:57], v[58:59]
	v_pk_add_f32 v[60:61], v[60:61], v[62:63]
	v_pk_add_f32 v[56:57], v[56:57], v[60:61]
	v_add_f32_e32 v50, v56, v57
	v_mov_b32_e32 v51, v50
	s_nop 1
	v_permlane32_swap_b32_e32 v50, v51
	v_add_f32_e32 v50, v50, v51
	v_log_f32_e32 v50, v50
	v_cvt_pk_f16_f32 v40, v18, v19
	v_cvt_pk_f16_f32 v41, v20, v21
	v_cvt_pk_f16_f32 v42, v22, v23
	v_cvt_pk_f16_f32 v43, v24, v25
	v_cvt_pk_f16_f32 v44, v26, v27
	v_cvt_pk_f16_f32 v45, v28, v29
	v_cvt_pk_f16_f32 v46, v30, v31
	v_cvt_pk_f16_f32 v47, v32, v33
	v_add_f32_e32 v50, 0x41600000, v50
	v_mul_f32_e32 v50, 0xbf317218, v50
	v_cndmask_b32_e64 v51, v50, 1.0, vcc
	s_waitcnt vmcnt(0)
	ds_read_b128 v[2:5], v39
	ds_read_b128 v[6:9], v81
	ds_read_b128 v[10:13], v82
	ds_read_b128 v[14:17], v83
	s_waitcnt lgkmcnt(2)
	v_max3_f32 v52, v2, v3, v4
	v_max3_f32 v53, v5, v6, v7
	v_max_f32_e32 v52, v52, v8
	v_max_f32_e32 v53, v53, v9
	s_waitcnt lgkmcnt(0)
	v_max3_f32 v52, v52, v10, v11
	v_max3_f32 v53, v53, v12, v13
	v_max3_f32 v52, v52, v14, v15
	v_max3_f32 v53, v53, v16, v17
	v_max_f32_e32 v52, v52, v53
	v_mov_b32_e32 v53, v52
	s_nop 1
	v_permlane32_swap_b32_e32 v52, v53
	v_max_f32_e32 v52, v52, v53
	v_cndmask_b32_e32 v54, 1.0, v52, vcc
	v_fmamk_f32 v48, v52, 0x3fb8aa3b, v34
	v_pk_fma_f32 v[2:3], v[2:3], v[84:85], v[48:49] op_sel_hi:[1,0,0] neg_lo:[0,0,1] neg_hi:[0,0,1]
	v_mfma_f32_32x32x2_f32 v[64:79], v54, v51, 0
	v_exp_f32_e32 v2, v2
	v_exp_f32_e32 v3, v3
	v_pk_fma_f32 v[4:5], v[4:5], v[84:85], v[48:49] op_sel_hi:[1,0,0] neg_lo:[0,0,1] neg_hi:[0,0,1]
	v_exp_f32_e32 v4, v4
	v_exp_f32_e32 v5, v5
	v_pk_fma_f32 v[6:7], v[6:7], v[84:85], v[48:49] op_sel_hi:[1,0,0] neg_lo:[0,0,1] neg_hi:[0,0,1]
	v_exp_f32_e32 v6, v6
	v_exp_f32_e32 v7, v7
	v_pk_fma_f32 v[8:9], v[8:9], v[84:85], v[48:49] op_sel_hi:[1,0,0] neg_lo:[0,0,1] neg_hi:[0,0,1]
	v_exp_f32_e32 v8, v8
	v_exp_f32_e32 v9, v9
	v_pk_fma_f32 v[10:11], v[10:11], v[84:85], v[48:49] op_sel_hi:[1,0,0] neg_lo:[0,0,1] neg_hi:[0,0,1]
	v_exp_f32_e32 v10, v10
	v_cvt_pk_f16_f32 v56, v2, v3
	v_cvt_pk_f16_f32 v57, v4, v5
	v_cvt_pk_f16_f32 v58, v6, v7
	v_cvt_pk_f16_f32 v59, v8, v9
	v_exp_f32_e32 v11, v11
	v_pk_fma_f32 v[12:13], v[12:13], v[84:85], v[48:49] op_sel_hi:[1,0,0] neg_lo:[0,0,1] neg_hi:[0,0,1]
	v_exp_f32_e32 v12, v12
	v_mfma_f32_32x32x16_f16 v[18:33], v[56:59], v[40:43], 0
	v_exp_f32_e32 v13, v13
	v_pk_fma_f32 v[14:15], v[14:15], v[84:85], v[48:49] op_sel_hi:[1,0,0] neg_lo:[0,0,1] neg_hi:[0,0,1]
	v_exp_f32_e32 v14, v14
	v_exp_f32_e32 v15, v15
	v_pk_fma_f32 v[16:17], v[16:17], v[84:85], v[48:49] op_sel_hi:[1,0,0] neg_lo:[0,0,1] neg_hi:[0,0,1]
	v_exp_f32_e32 v16, v16
	v_exp_f32_e32 v17, v17
	v_cvt_pk_f16_f32 v60, v10, v11
	v_cvt_pk_f16_f32 v61, v12, v13
	v_cvt_pk_f16_f32 v62, v14, v15
	v_cvt_pk_f16_f32 v63, v16, v17
	s_nop 1
	v_mfma_f32_32x32x16_f16 v[18:33], v[60:63], v[44:47], v[18:33]
	s_nop 11
	v_log_f32_e32 v18, v18
	v_log_f32_e32 v19, v19
	v_log_f32_e32 v20, v20
	v_log_f32_e32 v21, v21
	v_log_f32_e32 v22, v22
	v_log_f32_e32 v23, v23
	v_pk_fma_f32 v[64:65], v[18:19], v[84:85], v[64:65] op_sel:[0,1,0] op_sel_hi:[1,1,1]
	buffer_store_dword v64, v36, s[8:11], 0 offen
	buffer_store_dword v65, v36, s[8:11], s24 offen
	v_log_f32_e32 v24, v24
	v_log_f32_e32 v25, v25
	v_pk_fma_f32 v[66:67], v[20:21], v[84:85], v[66:67] op_sel:[0,1,0] op_sel_hi:[1,1,1]
	buffer_store_dword v66, v36, s[8:11], s25 offen
	buffer_store_dword v67, v36, s[8:11], s26 offen
	v_log_f32_e32 v26, v26
	v_log_f32_e32 v27, v27
	v_pk_fma_f32 v[68:69], v[22:23], v[84:85], v[68:69] op_sel:[0,1,0] op_sel_hi:[1,1,1]
	buffer_store_dword v68, v36, s[8:11], s27 offen
	buffer_store_dword v69, v36, s[8:11], s28 offen
	v_log_f32_e32 v28, v28
	v_log_f32_e32 v29, v29
	v_pk_fma_f32 v[70:71], v[24:25], v[84:85], v[70:71] op_sel:[0,1,0] op_sel_hi:[1,1,1]
	buffer_store_dword v70, v36, s[8:11], s29 offen
	buffer_store_dword v71, v36, s[8:11], s30 offen
	v_log_f32_e32 v30, v30
	v_log_f32_e32 v31, v31
	v_pk_fma_f32 v[72:73], v[26:27], v[84:85], v[72:73] op_sel:[0,1,0] op_sel_hi:[1,1,1]
	buffer_store_dword v72, v36, s[8:11], s31 offen
	buffer_store_dword v73, v36, s[8:11], s32 offen
	v_log_f32_e32 v32, v32
	v_log_f32_e32 v33, v33
	v_pk_fma_f32 v[74:75], v[28:29], v[84:85], v[74:75] op_sel:[0,1,0] op_sel_hi:[1,1,1]
	buffer_store_dword v74, v36, s[8:11], s33 offen
	buffer_store_dword v75, v36, s[8:11], s34 offen
	v_pk_fma_f32 v[76:77], v[30:31], v[84:85], v[76:77] op_sel:[0,1,0] op_sel_hi:[1,1,1]
	buffer_store_dword v76, v36, s[8:11], s35 offen
	buffer_store_dword v77, v36, s[8:11], s36 offen
	v_pk_fma_f32 v[78:79], v[32:33], v[84:85], v[78:79] op_sel:[0,1,0] op_sel_hi:[1,1,1]
	buffer_store_dword v78, v36, s[8:11], s37 offen
	buffer_store_dword v79, v36, s[8:11], s38 offen
	s_endpgm

	.amdhsa_kernel _Z16sum_layer_kernelPKfS0_Pf
		.amdhsa_group_segment_fixed_size 18432
		.amdhsa_private_segment_fixed_size 0
		.amdhsa_kernarg_size 24
		.amdhsa_user_sgpr_count 2
		.amdhsa_user_sgpr_dispatch_ptr 0
		.amdhsa_user_sgpr_queue_ptr 0
		.amdhsa_user_sgpr_kernarg_segment_ptr 1
		.amdhsa_user_sgpr_dispatch_id 0
		.amdhsa_user_sgpr_kernarg_preload_length 0
		.amdhsa_user_sgpr_kernarg_preload_offset 0
		.amdhsa_user_sgpr_private_segment_size 0
		.amdhsa_uses_dynamic_stack 0
		.amdhsa_enable_private_segment 0
		.amdhsa_system_sgpr_workgroup_id_x 1
		.amdhsa_system_sgpr_workgroup_id_y 0
		.amdhsa_system_sgpr_workgroup_id_z 0
		.amdhsa_system_sgpr_workgroup_info 0
		.amdhsa_system_vgpr_workitem_id 0
		.amdhsa_next_free_vgpr 88
		.amdhsa_next_free_sgpr 43
		.amdhsa_accum_offset 88
		.amdhsa_reserve_vcc 1
		.amdhsa_float_round_mode_32 0
		.amdhsa_float_round_mode_16_64 0
		.amdhsa_float_denorm_mode_32 3
		.amdhsa_float_denorm_mode_16_64 3
		.amdhsa_dx10_clamp 1
		.amdhsa_ieee_mode 1
		.amdhsa_fp16_overflow 0
		.amdhsa_tg_split 0
		.amdhsa_exception_fp_ieee_invalid_op 0
		.amdhsa_exception_fp_denorm_src 0
		.amdhsa_exception_fp_ieee_div_zero 0
		.amdhsa_exception_fp_ieee_overflow 0
		.amdhsa_exception_fp_ieee_underflow 0
		.amdhsa_exception_fp_ieee_inexact 0
		.amdhsa_exception_int_div_zero 0
	.end_amdhsa_kernel

amdhsa.kernels:
  - .agpr_count:     0
    .args:
      - .address_space:  global
        .offset:         0
        .size:           8
        .value_kind:     global_buffer
      - .address_space:  global
        .offset:         8
        .size:           8
        .value_kind:     global_buffer
      - .address_space:  global
        .offset:         16
        .size:           8
        .value_kind:     global_buffer
    .group_segment_fixed_size: 18432
    .kernarg_segment_align: 8
    .kernarg_segment_size: 24
    .language:       OpenCL C
    .language_version:
      - 2
      - 0
    .max_flat_workgroup_size: 256
    .name:           _Z16sum_layer_kernelPKfS0_Pf
    .private_segment_fixed_size: 0
    .sgpr_count:     49
    .sgpr_spill_count: 0
    .symbol:         _Z16sum_layer_kernelPKfS0_Pf.kd
    .uniform_work_group_size: 1
    .uses_dynamic_stack: false
    .vgpr_count:     88
    .vgpr_spill_count: 0
    .wavefront_size: 64
